# rwkv_out: second raw tile (Yloc) requested together with the first (V): one round trip less per unit
# speedup vs baseline: 1.0042x; 1.0042x over previous
; #define LAS __attribute__((address_space(3)))
; __device__ __forceinline__ int lt_tid(int wv) { int ln; asm volatile("v_mbcnt_lo_u32_b32 %0, -1, 0\n\tv_mbcnt_hi_u32_b32 %0, -1, %0" : "=v"(ln)); return (wv << 6) | ln; }
; __device__ __forceinline__ void ph_rwkv_out(const Params& p, int l, LAS unsigned char* lds, const int wvid) {
;     ...
;         int unit = rnd == 0 ? bid * NWAVE + wave : (((bid & 7) == 0 && wave == 0) ? (int)gridDim.x * NWAVE + (bid >> 3) : RUN);
;         if (unit >= RUN) continue;
;         if (bal) unit = (unit >> 6) * RCH + 1 + (unit & 63);
;         const int lane = lt_tid(wvid) & 63, l31 = lane & 31, hi = lane >> 5;
;         const int bh = unit / RCH, ch = unit % RCH, b = bh >> 2, h = bh & 3, t0 = ch * 64;
;         const size_t uo = (size_t)unit * 4096;
;         const bf16_t* GTg = (const bf16_t*)(ws + WS_RWB + RW_GT) + uo; const bf16_t* YLg = (const bf16_t*)(ws + WS_RWB + RW_YL) + uo; const bf16_t* VVg = (const bf16_t*)(ob + RO_VV) + uo;
;         const u32x4* SH = (const u32x4*)(ob + RO_SH) + (size_t)unit * 512;
;         LAS unsigned char* X = lds + wave * (2 * R2_MB); LAS unsigned char* Y = X + R2_MB;
;         R2_RAW(X, VVg); R2_RAW(Y, YLg);
;         bf16x8 ga[4][2], sb[4][2]; unsigned short yl[2][2][16];
; #pragma unroll
;         for (int ks = 0; ks < 4; ++ks)
; #pragma unroll
;             for (int x = 0; x < 2; ++x) { ga[ks][x] = *(const bf16x8*)(GTg + TM(32 * x + l31, 16 * ks + 8 * hi)); sb[ks][x] = __builtin_bit_cast(bf16x8, SH[(x * 4 + ks) * 64 + lane]); }
; #pragma unroll
;         for (int rb = 0; rb < 2; ++rb)
; #pragma unroll
;             for (int cb = 0; cb < 2; ++cb)
; #pragma unroll
;                 for (int r = 0; r < 16; ++r) yl[rb][cb][r] = (unsigned short)R2_RD16(Y, 32 * rb + (r & 3) + 8 * (r >> 2) + 4 * hi, 32 * cb + l31);
.LBB0_856:
	s_mul_hi_i32 s1, s0, 0x7e07e07f
	s_lshr_b32 s6, s1, 31
	s_ashr_i32 s1, s1, 5
	s_add_i32 s8, s1, s6
	s_mul_i32 s1, s8, 0x41
	s_sub_i32 s16, s0, s1
	s_ashr_i32 s1, s0, 31
	s_and_b32 s9, s8, 3
	s_lshl_b64 s[0:1], s[0:1], 13
	s_add_u32 s6, s20, s0
	v_mbcnt_lo_u32_b32 v0, -1, 0
	v_mbcnt_hi_u32_b32 v0, -1, v0
	s_addc_u32 s7, s21, s1
	v_and_b32_e32 v34, 63, v0
	s_add_u32 s10, s30, s0
	s_waitcnt lgkmcnt(11)
	v_lshlrev_b32_e32 v90, 4, v34
	s_addc_u32 s11, s31, s1
	s_waitcnt lgkmcnt(2)
	v_or_b32_e32 v35, 0x1000, v90
	v_or_b32_e32 v37, 0x1800, v90
	global_load_dwordx4 v[2:5], v90, s[10:11]
	global_load_dwordx4 v[6:9], v90, s[10:11] offset:1024
	global_load_dwordx4 v[10:13], v90, s[10:11] offset:2048
	global_load_dwordx4 v[14:17], v90, s[10:11] offset:3072
	v_or_b32_e32 v36, 0x1400, v90
	global_load_dwordx4 v[18:21], v35, s[10:11]
	global_load_dwordx4 v[22:25], v36, s[10:11]
	v_or_b32_e32 v38, 0x1c00, v90
	global_load_dwordx4 v[26:29], v37, s[10:11]
	global_load_dwordx4 v[30:33], v38, s[10:11]
	v_lshlrev_b32_e32 v39, 4, v0
	v_bfe_u32 v40, v0, 1, 5
	v_or_b32_e32 v34, 64, v34
	v_and_b32_e32 v39, 16, v39
	v_mul_u32_u24_e32 v40, 0x90, v40
	v_lshrrev_b32_e32 v34, 1, v34
	v_add3_u32 v40, s34, v40, v39
	v_mul_u32_u24_e32 v34, 0x90, v34
	s_ashr_i32 s8, s8, 2
	v_add3_u32 v39, s34, v34, v39
	s_add_u32 s10, s28, s0
	s_addc_u32 s11, s29, s1
	s_waitcnt vmcnt(33)
	v_bfe_u32 v103, v0, 5, 1
	s_waitcnt vmcnt(28)
	v_lshlrev_b32_e32 v96, 2, v103
	s_lshl_b32 s35, s16, 6
	v_or_b32_e32 v110, 32, v96
	v_mov_b32_e32 v34, 0x5a0
	s_add_u32 s0, s2, s0
	s_waitcnt vmcnt(24)
	global_load_dwordx4 v[200:203], v90, s[10:11]
	global_load_dwordx4 v[206:209], v90, s[10:11] offset:1024
	global_load_dwordx4 v[210:213], v90, s[10:11] offset:2048
	global_load_dwordx4 v[232:235], v90, s[10:11] offset:3072
	global_load_dwordx4 v[236:239], v35, s[10:11]
	global_load_dwordx4 v[240:243], v36, s[10:11]
	global_load_dwordx4 v[244:247], v37, s[10:11]
	global_load_dwordx4 v[196:199], v38, s[10:11]
	v_mov_b32_e32 v91, v1
	v_and_b32_e32 v100, 31, v0
	s_addc_u32 s1, s3, s1
	v_lshlrev_b32_e32 v0, 5, v100
	v_lshl_or_b32 v0, v103, 4, v0
	v_lshl_add_u64 v[94:95], s[6:7], 0, v[0:1]
	v_or_b32_e32 v98, 1, v96
	v_readlane_b32 s48, v253, 46
	v_readlane_b32 s49, v253, 47
	v_readlane_b32 s50, v253, 48
	v_readlane_b32 s51, v253, 49
	v_readlane_b32 s52, v253, 50
	v_readlane_b32 s53, v253, 51
	v_readlane_b32 s54, v253, 52
	v_readlane_b32 s55, v253, 53
	v_readlane_b32 s56, v253, 54
	v_readlane_b32 s57, v253, 55
	v_readlane_b32 s58, v253, 56
	v_readlane_b32 s59, v253, 57
	v_readlane_b32 s60, v253, 58
	v_readlane_b32 s61, v253, 59
	v_readlane_b32 s62, v253, 60
	v_readlane_b32 s63, v253, 61
	s_mov_b64 s[48:49], s[52:53]
	s_mov_b64 s[50:51], s[54:55]
	s_mov_b64 s[52:53], s[56:57]
	s_mov_b64 s[54:55], s[58:59]
	s_mov_b64 s[56:57], s[60:61]
	s_movk_i32 s70, 0x1000
	s_mov_b64 s[58:59], s[62:63]
	s_waitcnt vmcnt(15)
	ds_write_b128 v40, v[2:5]
	s_waitcnt vmcnt(14)
	ds_write_b128 v39, v[6:9]
	s_waitcnt vmcnt(13)
	ds_write_b128 v40, v[10:13] offset:32
	s_waitcnt vmcnt(12)
	ds_write_b128 v39, v[14:17] offset:32
	s_waitcnt vmcnt(11)
	ds_write_b128 v40, v[18:21] offset:64
	s_waitcnt vmcnt(10)
	ds_write_b128 v40, v[22:25] offset:4672
	s_waitcnt vmcnt(9)
	ds_write_b128 v40, v[26:29] offset:96
	s_waitcnt vmcnt(8)
	ds_write_b128 v40, v[30:33] offset:4704
	v_mad_u32_u24 v37, v110, s83, v34
	v_mov_b32_e32 v34, 0xab0
	v_mad_u32_u24 v38, v110, s83, v34
	v_lshl_add_u64 v[34:35], s[0:1], 0, v[90:91]
	s_movk_i32 s10, 0x1000
	v_add_co_u32_e32 v92, vcc, s10, v34
	v_mad_u32_u24 v36, v110, s83, s83
	s_nop 0
	v_addc_co_u32_e32 v93, vcc, 0, v35, vcc
	v_add_co_u32_e32 v94, vcc, s10, v94
	s_waitcnt vmcnt(7)
	ds_write_b128 v40, v[200:203] offset:9216
	s_waitcnt vmcnt(6)
	ds_write_b128 v39, v[206:209] offset:9216
	s_waitcnt vmcnt(5)
	ds_write_b128 v40, v[210:213] offset:9248
	s_waitcnt vmcnt(4)
	ds_write_b128 v39, v[232:235] offset:9248
	s_waitcnt vmcnt(3)
	ds_write_b128 v40, v[236:239] offset:9280
	s_waitcnt vmcnt(2)
	ds_write_b128 v40, v[240:243] offset:13888
	s_waitcnt vmcnt(1)
	ds_write_b128 v40, v[244:247] offset:9312
	s_waitcnt vmcnt(0)
	ds_write_b128 v40, v[196:199] offset:13920
	global_load_dwordx4 v[20:23], v0, s[6:7]
	global_load_dwordx4 v[78:81], v0, s[6:7] offset:1024
	global_load_dwordx4 v[28:31], v90, s[0:1]
	global_load_dwordx4 v[74:77], v90, s[0:1] offset:1024
	global_load_dwordx4 v[82:85], v0, s[6:7] offset:2048
	global_load_dwordx4 v[66:69], v0, s[6:7] offset:3072
	global_load_dwordx4 v[86:89], v[92:93], off
	global_load_dwordx4 v[70:73], v[92:93], off offset:1024
	v_lshlrev_b32_e32 v0, 1, v100
	v_add_u32_e32 v111, s34, v0
	s_movk_i32 s6, 0x240
	v_mad_u32_u24 v2, v103, s6, v111
	v_mad_u32_u24 v148, v98, s83, v111
	v_mad_u32_u24 v3, v110, s83, v111
	v_add_u32_e32 v114, v111, v36
	v_add_u32_e32 v113, v111, v37
	v_add_u32_e32 v112, v111, v38
	ds_read_u16 v4, v148 offset:9216
	ds_read_u16 v5, v148 offset:9360
	ds_read_u16 v6, v148 offset:9504
	ds_read_u16 v7, v148 offset:10224
	ds_read_u16 v8, v148 offset:10288
	ds_read_u16 v9, v148 offset:9568
	ds_read_u16 v10, v148 offset:9424
	ds_read_u16 v11, v148 offset:9280
	ds_read_u16 v12, v148 offset:10368
	ds_read_u16 v13, v148 offset:10512
	ds_read_u16 v14, v148 offset:10656
	ds_read_u16 v15, v148 offset:11376
	ds_read_u16 v16, v148 offset:11440
	ds_read_u16 v17, v148 offset:10720
	ds_read_u16 v18, v148 offset:10576
	ds_read_u16 v19, v148 offset:10432
	ds_read_u16 v24, v148 offset:11520
	ds_read_u16 v25, v148 offset:11664
	ds_read_u16 v26, v148 offset:11808
	ds_read_u16 v27, v148 offset:12528
	ds_read_u16 v32, v148 offset:12592
	ds_read_u16 v33, v148 offset:11872
; __device__ __forceinline__ float bf2f(bf16_t b) { return __uint_as_float(((unsigned)b) << 16); }
; __device__ __forceinline__ void ph_rwkv_out(const Params& p, int l, LAS unsigned char* lds, const int wvid) {
;     ...
;                 for (int r = 0; r < 16; ++r) yl[rb][cb][r] = (unsigned short)R2_RD16(Y, 32 * rb + (r & 3) + 8 * (r >> 2) + 4 * hi, 32 * cb + l31);
;         M64 Yt;
; #pragma unroll
;         for (int rb = 0; rb < 2; ++rb)
; #pragma unroll
;             for (int cb = 0; cb < 2; ++cb)
; #pragma unroll
;                 for (int r = 0; r < 16; ++r) Yt[rb][cb][r] = bf2f(yl[rb][cb][r]);
; #pragma unroll
;         for (int ks = 0; ks < 4; ++ks)
; #pragma unroll
;             for (int rb = 0; rb < 2; ++rb)
; #pragma unroll
;                 for (int cb = 0; cb < 2; ++cb) Yt[rb][cb] = __builtin_amdgcn_mfma_f32_32x32x16_bf16(ga[ks][rb], sb[ks][cb], Yt[rb][cb], 0, 0, 0);
;         const float lg0 = p.in[I_LNXG][l * 256 + h * 64 + l31], lg1 = p.in[I_LNXG][l * 256 + h * 64 + 32 + l31], lb0 = p.in[I_LNXB][l * 256 + h * 64 + l31], lb1 = p.in[I_LNXB][l * 256 + h * 64 + 32 + l31];
	ds_read_u16 v60, v148 offset:11728
	ds_read_u16 v58, v148 offset:11584
	ds_read_u16 v46, v148 offset:12672
	ds_read_u16 v48, v148 offset:12816
	ds_read_u16 v49, v148 offset:12960
	ds_read_u16 v64, v148 offset:13024
	ds_read_u16 v102, v3 offset:9216
	ds_read_u16 v104, v3 offset:9280
	ds_read_u16 v3, v148 offset:12880
	ds_read_u16 v62, v148 offset:12736
	ds_read_u16 v106, v114 offset:9216
	ds_read_u16 v107, v114 offset:9360
	ds_read_u16 v108, v114 offset:9504
	ds_read_u16 v109, v114 offset:10224
	ds_read_u16 v115, v114 offset:10288
	ds_read_u16 v116, v114 offset:9568
	ds_read_u16 v117, v114 offset:9424
	ds_read_u16 v118, v114 offset:9280
	ds_read_u16 v119, v114 offset:10368
	ds_read_u16 v120, v113 offset:9216
	ds_read_u16 v121, v113 offset:9360
	ds_read_u16 v122, v113 offset:10080
	ds_read_u16 v123, v113 offset:10144
	ds_read_u16 v124, v113 offset:9424
	ds_read_u16 v125, v113 offset:9280
	ds_read_u16 v126, v114 offset:10432
	ds_read_u16 v127, v113 offset:10224
	ds_read_u16 v128, v113 offset:10368
	ds_read_u16 v129, v112 offset:9216
	ds_read_u16 v130, v112 offset:9936
	ds_read_u16 v131, v112 offset:10000
	ds_read_u16 v132, v112 offset:9280
	ds_read_u16 v133, v113 offset:10432
	ds_read_u16 v134, v113 offset:10288
	ds_read_u16 v135, v112 offset:10080
	ds_read_u16 v136, v112 offset:10224
	ds_read_u16 v137, v112 offset:10368
	ds_read_u16 v138, v112 offset:10432
	ds_read_u16 v139, v112 offset:10288
	ds_read_u16 v140, v112 offset:10144
	ds_read_u16 v34, v2 offset:9216
	ds_read_u16 v2, v2 offset:9280
	ds_read_u16 v141, v148
	ds_read_u16 v105, v148 offset:64
	ds_read_u16 v101, v148 offset:144
	ds_read_u16 v99, v148 offset:208
	ds_read_u16 v97, v148 offset:288
	ds_read_u16 v91, v148 offset:352
	s_waitcnt lgkmcnt(14)
	v_lshlrev_b32_e32 v35, 16, v4
	s_waitcnt lgkmcnt(7)
	v_lshlrev_b32_e32 v34, 16, v34
	v_lshlrev_b32_e32 v37, 16, v6
	v_lshlrev_b32_e32 v36, 16, v5
	v_lshlrev_b32_e32 v39, 16, v12
	v_lshlrev_b32_e32 v38, 16, v7
	v_lshlrev_b32_e32 v41, 16, v14
	v_lshlrev_b32_e32 v40, 16, v13
	v_lshlrev_b32_e32 v43, 16, v24
	v_lshlrev_b32_e32 v42, 16, v15
	v_lshlrev_b32_e32 v45, 16, v26
	v_lshlrev_b32_e32 v44, 16, v25
	v_lshlrev_b32_e32 v47, 16, v46
	v_lshlrev_b32_e32 v46, 16, v27
	v_lshlrev_b32_e32 v49, 16, v49
	v_lshlrev_b32_e32 v48, 16, v48
	v_lshlrev_b32_e32 v51, 16, v11
	s_waitcnt lgkmcnt(6)
	v_lshlrev_b32_e32 v50, 16, v2
	v_lshlrev_b32_e32 v53, 16, v9
	v_lshlrev_b32_e32 v52, 16, v10
	v_lshlrev_b32_e32 v54, 16, v8
	v_lshlrev_b32_e32 v57, 16, v17
	v_lshlrev_b32_e32 v59, 16, v58
	v_lshlrev_b32_e32 v58, 16, v16
	v_lshlrev_b32_e32 v65, 16, v64
	v_lshlrev_b32_e32 v64, 16, v3
	v_lshlrev_b32_e32 v3, 16, v106
	v_lshlrev_b32_e32 v2, 16, v102
	v_lshlrev_b32_e32 v5, 16, v108
	v_lshlrev_b32_e32 v4, 16, v107
	v_lshlrev_b32_e32 v7, 16, v119
	v_lshlrev_b32_e32 v6, 16, v109
	v_lshlrev_b32_e32 v9, 16, v121
	v_lshlrev_b32_e32 v8, 16, v120
	v_lshlrev_b32_e32 v11, 16, v127
	v_lshlrev_b32_e32 v10, 16, v122
	v_lshlrev_b32_e32 v13, 16, v129
	v_lshlrev_b32_e32 v12, 16, v128
	v_lshlrev_b32_e32 v15, 16, v135
	v_lshlrev_b32_e32 v14, 16, v130
	v_lshlrev_b32_e32 v17, 16, v137
	v_lshlrev_b32_e32 v16, 16, v136
	v_lshlrev_b32_e32 v55, 16, v19
	v_lshlrev_b32_e32 v56, 16, v18
	v_lshlrev_b32_e32 v61, 16, v33
	v_lshlrev_b32_e32 v60, 16, v60
	v_lshlrev_b32_e32 v63, 16, v62
	v_lshlrev_b32_e32 v62, 16, v32
	v_lshlrev_b32_e32 v19, 16, v118
	v_lshlrev_b32_e32 v18, 16, v104
	v_lshlrev_b32_e32 v25, 16, v124
	v_lshlrev_b32_e32 v24, 16, v125
	s_waitcnt vmcnt(5)
	v_mfma_f32_32x32x16_bf16 v[34:49], v[20:23], v[28:31], v[34:49]
	v_lshlrev_b32_e32 v27, 16, v134
	v_lshlrev_b32_e32 v26, 16, v123
	v_lshlrev_b32_e32 v33, 16, v138
	v_lshlrev_b32_e32 v32, 16, v139
	v_addc_co_u32_e32 v95, vcc, 0, v95, vcc
	v_cmp_gt_u32_e32 vcc, 32, v222
	v_mfma_f32_32x32x16_bf16 v[2:17], v[78:81], v[28:31], v[2:17]
	v_lshlrev_b32_e32 v29, 16, v132
	v_lshlrev_b32_e32 v28, 16, v133
	v_lshlrev_b32_e32 v31, 16, v140
	v_lshlrev_b32_e32 v30, 16, v131
	s_waitcnt vmcnt(1)
	v_mfma_f32_32x32x16_bf16 v[50:65], v[20:23], v[86:89], v[50:65]
	v_lshlrev_b32_e32 v21, 16, v116
	v_lshlrev_b32_e32 v20, 16, v117
	v_lshlrev_b32_e32 v23, 16, v126
	v_lshlrev_b32_e32 v22, 16, v115
	s_nop 1
	v_mfma_f32_32x32x16_bf16 v[18:33], v[78:81], v[86:89], v[18:33]
	v_mfma_f32_32x32x16_bf16 v[34:49], v[82:85], v[74:77], v[34:49]
	v_mfma_f32_32x32x16_bf16 v[2:17], v[66:69], v[74:77], v[2:17]
	global_load_dwordx4 v[74:77], v[94:95], off
	s_waitcnt vmcnt(1)
	v_mfma_f32_32x32x16_bf16 v[50:65], v[82:85], v[70:73], v[50:65]
	v_mfma_f32_32x32x16_bf16 v[18:33], v[66:69], v[70:73], v[18:33]
	global_load_dwordx4 v[70:73], v90, s[0:1] offset:2048
	global_load_dwordx4 v[78:81], v[94:95], off offset:1024
	global_load_dwordx4 v[82:85], v90, s[0:1] offset:3072
	global_load_dwordx4 v[86:89], v[92:93], off offset:2048
	global_load_dwordx4 v[66:69], v[92:93], off offset:3072
	s_lshl_b32 s0, s9, 7
	s_add_u32 s6, s22, s0
	s_addc_u32 s7, s23, 0
	s_lshl_b32 s1, s9, 2
	s_add_u32 s10, s24, s1
	s_addc_u32 s11, s25, 0
	s_waitcnt vmcnt(4)
	v_mfma_f32_32x32x16_bf16 v[34:49], v[74:77], v[70:73], v[34:49]
	s_waitcnt vmcnt(1)
	v_mfma_f32_32x32x16_bf16 v[50:65], v[74:77], v[86:89], v[50:65]
	global_load_dwordx4 v[74:77], v[94:95], off offset:2048
	v_mfma_f32_32x32x16_bf16 v[2:17], v[78:81], v[70:73], v[2:17]
	global_load_dwordx4 v[70:73], v[94:95], off offset:3072
	v_mfma_f32_32x32x16_bf16 v[18:33], v[78:81], v[86:89], v[18:33]
	v_or_b32_e32 v78, s40, v100
	v_mov_b32_e32 v79, v1
	v_lshl_or_b32 v78, s9, 6, v78
	v_lshlrev_b64 v[78:79], 2, v[78:79]
	v_lshl_add_u64 v[80:81], s[54:55], 0, v[78:79]
	v_lshl_add_u64 v[78:79], s[56:57], 0, v[78:79]
	global_load_dword v109, v[80:81], off
	global_load_dword v107, v[80:81], off offset:128
	global_load_dword v108, v[78:79], off
	global_load_dword v106, v[78:79], off offset:128
	s_waitcnt vmcnt(5)
; __device__ __forceinline__ void ph_rwkv_out(const Params& p, int l, LAS unsigned char* lds, const int wvid) {
;     ...
;                 for (int cb = 0; cb < 2; ++cb) Yt[rb][cb] = __builtin_amdgcn_mfma_f32_32x32x16_bf16(ga[ks][rb], sb[ks][cb], Yt[rb][cb], 0, 0, 0);
;         const float lg0 = p.in[I_LNXG][l * 256 + h * 64 + l31], lg1 = p.in[I_LNXG][l * 256 + h * 64 + 32 + l31], lb0 = p.in[I_LNXB][l * 256 + h * 64 + l31], lb1 = p.in[I_LNXB][l * 256 + h * 64 + 32 + l31];
; #pragma unroll
;         for (int rb = 0; rb < 2; ++rb) {
;             unsigned short v0[16], v1[16], g0[16], g1[16]; float bcv[16];
; #pragma unroll
;             for (int r = 0; r < 16; ++r) { const int t = 32 * rb + (r & 3) + 8 * (r >> 2) + 4 * hi; const int tg = min(t0 + t, LT - 1); const size_t row = (size_t)b * LT + tg;
;                 v0[r] = (unsigned short)R2_RD16(X, t, l31); v1[r] = (unsigned short)R2_RD16(X, t, 32 + l31); g0[r] = Gg[row * 256 + h * 64 + l31]; g1[r] = Gg[row * 256 + h * 64 + 32 + l31]; bcv[r] = BCg[row * 4 + h]; }
	v_mfma_f32_32x32x16_bf16 v[34:49], v[74:77], v[82:85], v[34:49]
	s_mul_hi_i32 s9, s8, 0x1010
	v_mfma_f32_32x32x16_bf16 v[50:65], v[74:77], v[66:69], v[50:65]
	v_or_b32_e32 v76, s35, v96
	v_or_b32_e32 v77, s35, v98
	v_or_b32_e32 v102, 3, v76
	v_min_i32_e32 v78, 0x100f, v77
	v_or_b32_e32 v104, 2, v76
	v_min_i32_e32 v86, 0x100f, v102
	v_ashrrev_i32_e32 v79, 31, v78
	s_waitcnt vmcnt(4)
	v_mfma_f32_32x32x16_bf16 v[2:17], v[70:73], v[82:85], v[2:17]
	v_min_i32_e32 v82, 0x100f, v104
	v_ashrrev_i32_e32 v87, 31, v86
	v_lshl_add_u64 v[74:75], s[6:7], 0, v[0:1]
	v_mad_i64_i32 v[78:79], s[6:7], s8, v251, v[78:79]
	v_ashrrev_i32_e32 v83, 31, v82
	v_mad_i64_i32 v[86:87], s[6:7], s8, v251, v[86:87]
	v_lshlrev_b64 v[80:81], 9, v[78:79]
	v_mad_i64_i32 v[82:83], s[6:7], s8, v251, v[82:83]
	v_lshlrev_b64 v[88:89], 9, v[86:87]
	v_lshl_add_u64 v[80:81], v[74:75], 0, v[80:81]
	v_lshlrev_b64 v[84:85], 9, v[82:83]
	v_lshl_add_u64 v[88:89], v[74:75], 0, v[88:89]
	v_or_b32_e32 v96, 10, v76
	v_lshl_add_u64 v[78:79], v[78:79], 4, s[10:11]
	v_lshl_add_u64 v[84:85], v[74:75], 0, v[84:85]
	v_lshl_add_u64 v[82:83], v[82:83], 4, s[10:11]
	global_load_ushort v167, v[80:81], off
	global_load_ushort v165, v[80:81], off offset:64
	global_load_dword v166, v[78:79], off
	v_min_i32_e32 v196, 0x100f, v76
	v_ashrrev_i32_e32 v197, 31, v196
	v_mad_i64_i32 v[196:197], s[6:7], s8, v251, v[196:197]
	v_lshlrev_b64 v[198:199], 9, v[196:197]
	v_lshl_add_u64 v[198:199], v[74:75], 0, v[198:199]
	v_lshl_add_u64 v[196:197], v[196:197], 4, s[10:11]
	global_load_ushort v185, v[198:199], off
	global_load_ushort v186, v[198:199], off offset:64
	global_load_dword v184, v[196:197], off
	global_load_ushort v162, v[84:85], off
	global_load_ushort v160, v[84:85], off offset:64
	global_load_dword v161, v[82:83], off
	global_load_ushort v156, v[88:89], off
	global_load_ushort v155, v[88:89], off offset:64
	v_or_b32_e32 v100, 8, v76
	v_or_b32_e32 v98, 9, v76
	v_min_i32_e32 v88, 0x100f, v96
	v_min_i32_e32 v80, 0x100f, v100
	v_min_i32_e32 v84, 0x100f, v98
	v_ashrrev_i32_e32 v89, 31, v88
	v_ashrrev_i32_e32 v81, 31, v80
	v_ashrrev_i32_e32 v85, 31, v84
	v_mad_i64_i32 v[88:89], s[6:7], s8, v251, v[88:89]
	v_mad_i64_i32 v[80:81], s[6:7], s8, v251, v[80:81]
	v_mad_i64_i32 v[84:85], s[6:7], s8, v251, v[84:85]
	v_lshlrev_b64 v[92:93], 9, v[88:89]
	v_lshl_add_u64 v[78:79], v[86:87], 4, s[10:11]
	v_lshlrev_b64 v[82:83], 9, v[80:81]
	v_lshl_add_u64 v[80:81], v[80:81], 4, s[10:11]
	v_lshlrev_b64 v[86:87], 9, v[84:85]
	v_lshl_add_u64 v[84:85], v[84:85], 4, s[10:11]
	v_lshl_add_u64 v[116:117], v[74:75], 0, v[92:93]
	v_or_b32_e32 v94, 11, v76
	v_or_b32_e32 v92, 16, v76
	v_lshl_add_u64 v[82:83], v[74:75], 0, v[82:83]
	v_lshl_add_u64 v[86:87], v[74:75], 0, v[86:87]
	global_load_dword v159, v[78:79], off
	global_load_ushort v154, v[82:83], off
	global_load_ushort v152, v[82:83], off offset:64
	global_load_dword v153, v[80:81], off
	global_load_ushort v149, v[86:87], off
	global_load_ushort v146, v[86:87], off offset:64
	global_load_dword v147, v[84:85], off
	global_load_ushort v95, v[116:117], off
	v_min_i32_e32 v80, 0x100f, v94
	v_min_i32_e32 v84, 0x100f, v92
	v_ashrrev_i32_e32 v81, 31, v80
	v_ashrrev_i32_e32 v85, 31, v84
	v_mad_i64_i32 v[80:81], s[6:7], s8, v251, v[80:81]
	v_mad_i64_i32 v[84:85], s[6:7], s8, v251, v[84:85]
	v_lshlrev_b64 v[82:83], 9, v[80:81]
	v_lshlrev_b64 v[86:87], 9, v[84:85]
	v_lshl_add_u64 v[78:79], v[88:89], 4, s[10:11]
	v_lshl_add_u64 v[82:83], v[74:75], 0, v[82:83]
	v_lshl_add_u64 v[86:87], v[74:75], 0, v[86:87]
	v_or_b32_e32 v90, 17, v76
	v_or_b32_e32 v88, 18, v76
	v_lshl_add_u64 v[80:81], v[80:81], 4, s[10:11]
	v_lshl_add_u64 v[84:85], v[84:85], 4, s[10:11]
	global_load_ushort v142, v[116:117], off offset:64
	global_load_dword v143, v[78:79], off
	global_load_ushort v139, v[82:83], off
	global_load_ushort v93, v[82:83], off offset:64
	global_load_dword v137, v[80:81], off
	global_load_ushort v135, v[86:87], off
	global_load_ushort v132, v[86:87], off offset:64
	global_load_dword v133, v[84:85], off
	v_min_i32_e32 v78, 0x100f, v90
	v_min_i32_e32 v82, 0x100f, v88
	v_or_b32_e32 v86, 19, v76
	v_ashrrev_i32_e32 v79, 31, v78
	v_ashrrev_i32_e32 v83, 31, v82
	v_min_i32_e32 v116, 0x100f, v86
	v_mad_i64_i32 v[78:79], s[6:7], s8, v251, v[78:79]
	v_mad_i64_i32 v[82:83], s[6:7], s8, v251, v[82:83]
	v_ashrrev_i32_e32 v117, 31, v116
	v_lshlrev_b64 v[80:81], 9, v[78:79]
	v_lshlrev_b64 v[84:85], 9, v[82:83]
	v_mad_i64_i32 v[116:117], s[6:7], s8, v251, v[116:117]
	v_lshl_add_u64 v[80:81], v[74:75], 0, v[80:81]
	v_lshl_add_u64 v[84:85], v[74:75], 0, v[84:85]
	v_lshlrev_b64 v[118:119], 9, v[116:117]
	v_lshl_add_u64 v[78:79], v[78:79], 4, s[10:11]
	v_lshl_add_u64 v[82:83], v[82:83], 4, s[10:11]
	v_lshl_add_u64 v[118:119], v[74:75], 0, v[118:119]
	global_load_ushort v131, v[80:81], off
	global_load_ushort v89, v[80:81], off offset:64
	global_load_dword v130, v[78:79], off
	global_load_ushort v127, v[84:85], off
	global_load_ushort v87, v[84:85], off offset:64
	global_load_dword v126, v[82:83], off
	global_load_ushort v124, v[118:119], off
	s_nop 0
	global_load_ushort v85, v[118:119], off offset:64
	v_or_b32_e32 v84, 24, v76
	v_min_i32_e32 v80, 0x100f, v84
	v_ashrrev_i32_e32 v81, 31, v80
	v_mad_i64_i32 v[80:81], s[6:7], s8, v251, v[80:81]
	v_lshlrev_b64 v[82:83], 9, v[80:81]
	v_lshl_add_u64 v[78:79], v[116:117], 4, s[10:11]
	v_lshl_add_u64 v[116:117], v[74:75], 0, v[82:83]
	v_or_b32_e32 v82, 25, v76
; __device__ __forceinline__ float bf2f(bf16_t b) { return __uint_as_float(((unsigned)b) << 16); }
; __device__ __forceinline__ bf16_t f2bf(float f) { unsigned u = __float_as_uint(f); u += 0x7FFFu + ((u >> 16) & 1u); return (bf16_t)(u >> 16); }
; __device__ __forceinline__ float frsq(float x) { return __builtin_amdgcn_rsqf(x); }
; __device__ __forceinline__ float half_sum32(float v) {
;     v = row_sum16(v); v = dpp_add<0x142, 0xA>(v);
;     const float lo = __int_as_float(__builtin_amdgcn_readlane(__float_as_int(v), 31)), hi = __int_as_float(__builtin_amdgcn_readlane(__float_as_int(v), 63));
;     return (__builtin_amdgcn_mbcnt_hi(~0u, __builtin_amdgcn_mbcnt_lo(~0u, 0u)) < 32u) ? lo : hi;
; }
; __device__ __forceinline__ void ph_rwkv_out(const Params& p, int l, LAS unsigned char* lds, const int wvid) {
;     ...
;             for (int r = 0; r < 16; ++r) { const int t = 32 * rb + (r & 3) + 8 * (r >> 2) + 4 * hi; const int tg = min(t0 + t, LT - 1); const size_t row = (size_t)b * LT + tg;
;                 v0[r] = (unsigned short)R2_RD16(X, t, l31); v1[r] = (unsigned short)R2_RD16(X, t, 32 + l31); g0[r] = Gg[row * 256 + h * 64 + l31]; g1[r] = Gg[row * 256 + h * 64 + 32 + l31]; bcv[r] = BCg[row * 4 + h]; }
; #pragma unroll
;             for (int r = 0; r < 16; ++r) { const int t = 32 * rb + (r & 3) + 8 * (r >> 2) + 4 * hi, tg = t0 + t;
;                 const float y0 = Yt[rb][0][r], y1 = Yt[rb][1][r];
;                 const float mean = half_sum32(y0 + y1) * (1.f / 64.f); const float d0 = y0 - mean, d1 = y1 - mean;
;                 const float var = half_sum32(d0 * d0 + d1 * d1) * (1.f / 64.f); const float rs = frsq(var + 64e-5f);
;                 if (tg < LT) { const size_t row = (size_t)b * LT + tg;
;                     const float o0 = (d0 * rs * lg0 + lb0 + bcv[r] * bf2f(v0[r])) * bf2f(g0[r]);
;                     const float o1 = (d1 * rs * lg1 + lb1 + bcv[r] * bf2f(v1[r])) * bf2f(g1[r]);
;                     MIX[row * D + M_C + h * 64 + l31] = f2bf(o0); MIX[row * D + M_C + h * 64 + 32 + l31] = f2bf(o1); } }
	v_lshl_add_u64 v[118:119], v[80:81], 4, s[10:11]
	v_min_i32_e32 v80, 0x100f, v82
	v_ashrrev_i32_e32 v81, 31, v80
	v_mad_i64_i32 v[80:81], s[6:7], s8, v251, v[80:81]
	v_lshlrev_b64 v[120:121], 9, v[80:81]
	v_lshl_add_u64 v[144:145], v[80:81], 4, s[10:11]
	v_or_b32_e32 v80, 26, v76
	v_lshl_add_u64 v[128:129], v[74:75], 0, v[120:121]
	v_min_i32_e32 v120, 0x100f, v80
	v_ashrrev_i32_e32 v121, 31, v120
	v_mad_i64_i32 v[150:151], s[6:7], s8, v251, v[120:121]
	v_lshlrev_b64 v[120:121], 9, v[150:151]
	v_lshl_add_u64 v[168:169], v[74:75], 0, v[120:121]
	global_load_dword v125, v[78:79], off
	global_load_ushort v123, v[116:117], off
	global_load_ushort v83, v[116:117], off offset:64
	global_load_dword v122, v[118:119], off
	global_load_ushort v121, v[128:129], off
	global_load_ushort v81, v[128:129], off offset:64
	global_load_dword v120, v[144:145], off
	global_load_ushort v79, v[168:169], off
	v_or_b32_e32 v78, 27, v76
	v_min_i32_e32 v118, 0x100f, v78
	v_ashrrev_i32_e32 v119, 31, v118
	v_mad_i64_i32 v[118:119], s[6:7], s8, v251, v[118:119]
	v_lshl_add_u64 v[116:117], v[150:151], 4, s[10:11]
	v_lshlrev_b64 v[128:129], 9, v[118:119]
	v_lshl_add_u64 v[128:129], v[74:75], 0, v[128:129]
	v_lshl_add_u64 v[144:145], v[118:119], 4, s[10:11]
	global_load_ushort v118, v[168:169], off offset:64
	global_load_dword v119, v[116:117], off
	s_nop 0
	global_load_ushort v117, v[128:129], off
	global_load_ushort v115, v[128:129], off offset:64
	global_load_dword v116, v[144:145], off
	v_mfma_f32_32x32x16_bf16 v[18:33], v[70:73], v[66:69], v[18:33]
	ds_read_u16 v169, v148 offset:1008
	ds_read_u16 v168, v148 offset:1072
	ds_read_u16 v164, v148 offset:1152
	ds_read_u16 v163, v148 offset:1216
	ds_read_u16 v158, v148 offset:1296
	ds_read_u16 v157, v148 offset:1360
	ds_read_u16 v151, v148 offset:1440
	ds_read_u16 v150, v148 offset:1504
	ds_read_u16 v145, v148 offset:2160
	ds_read_u16 v144, v148 offset:2224
	ds_read_u16 v140, v148 offset:2304
	ds_read_u16 v138, v148 offset:2368
	ds_read_u16 v136, v148 offset:2448
	ds_read_u16 v134, v148 offset:2512
	ds_read_u16 v129, v148 offset:2592
	ds_read_u16 v128, v148 offset:2656
	ds_read_u16 v73, v148 offset:3312
	ds_read_u16 v72, v148 offset:3376
	ds_read_u16 v71, v148 offset:3456
	ds_read_u16 v70, v148 offset:3520
	ds_read_u16 v69, v148 offset:3600
	ds_read_u16 v68, v148 offset:3664
	ds_read_u16 v67, v148 offset:3744
	ds_read_u16 v66, v148 offset:3808
	v_add_f32_e32 v77, v34, v50
	v_mov_b32_e32 v148, v1
	s_add_u32 s6, s18, s0
	v_add_f32_dpp v77, v77, v77 quad_perm:[1,0,3,2] row_mask:0xf bank_mask:0xf bound_ctrl:1
	s_mulk_i32 s8, 0x1010
	s_addc_u32 s7, s19, 0
	v_add_f32_dpp v77, v77, v77 quad_perm:[2,3,0,1] row_mask:0xf bank_mask:0xf bound_ctrl:1
	s_nop 1
	v_add_f32_dpp v77, v77, v77 row_half_mirror row_mask:0xf bank_mask:0xf bound_ctrl:1
	s_nop 1
	v_add_f32_dpp v77, v77, v77 row_mirror row_mask:0xf bank_mask:0xf bound_ctrl:1
	s_nop 1
	v_mov_b32_dpp v148, v77 row_bcast:15 row_mask:0xa bank_mask:0xf
	v_add_f32_e32 v77, v77, v148
	s_nop 0
	v_readlane_b32 s0, v77, 31
	v_readlane_b32 s1, v77, 63
	s_nop 0
	v_mov_b32_e32 v148, s0
	v_mov_b32_e32 v77, s1
	v_cndmask_b32_e32 v77, v77, v148, vcc
	v_fmamk_f32 v148, v77, 0xbc800000, v34
	v_fmamk_f32 v34, v77, 0xbc800000, v50
	v_mul_f32_e32 v50, v34, v34
	v_fmac_f32_e32 v50, v148, v148
	v_mov_b32_e32 v77, v1
	v_cmp_gt_i32_e64 s[0:1], s33, v76
	v_add_f32_dpp v50, v50, v50 quad_perm:[1,0,3,2] row_mask:0xf bank_mask:0xf bound_ctrl:1
	s_nop 1
	v_add_f32_dpp v50, v50, v50 quad_perm:[2,3,0,1] row_mask:0xf bank_mask:0xf bound_ctrl:1
	s_nop 1
	v_add_f32_dpp v50, v50, v50 row_half_mirror row_mask:0xf bank_mask:0xf bound_ctrl:1
	s_nop 1
	v_add_f32_dpp v50, v50, v50 row_mirror row_mask:0xf bank_mask:0xf bound_ctrl:1
	s_nop 1
	v_mov_b32_dpp v77, v50 row_bcast:15 row_mask:0xa bank_mask:0xf
	v_add_f32_e32 v50, v50, v77
	s_nop 0
	v_readlane_b32 s36, v50, 31
	v_readlane_b32 s37, v50, 63
	s_and_saveexec_b64 s[16:17], s[0:1]
	s_cbranch_execz .LBB0_858
	v_ashrrev_i32_e32 v77, 31, v76
	v_lshl_add_u64 v[170:171], s[8:9], 0, v[76:77]
	v_lshl_add_u64 v[172:173], v[170:171], 4, s[10:11]
	s_nop 0
	v_mul_u32_u24_e32 v50, 0x240, v103
	v_mov_b32_e32 v103, s37
	v_mov_b32_e32 v174, s36
	v_cndmask_b32_e32 v103, v103, v174, vcc
	v_add_u32_e32 v50, v111, v50
	v_fmamk_f32 v103, v103, 0x3c800000, v249
	v_rsq_f32_e32 v103, v103
	ds_read_u16 v174, v50
	ds_read_u16 v50, v50 offset:64
	v_lshlrev_b64 v[172:173], 9, v[170:171]
	v_mul_f32_e32 v148, v148, v103
	v_lshl_add_u64 v[172:173], v[74:75], 0, v[172:173]
	s_waitcnt vmcnt(47)
	v_fma_f32 v148, v109, v148, v108
	s_waitcnt lgkmcnt(1)
	v_lshlrev_b32_e32 v174, 16, v174
	v_mul_f32_e32 v34, v34, v103
	s_waitcnt vmcnt(46)
	v_fma_f32 v34, v107, v34, v106
	s_waitcnt lgkmcnt(0)
	v_lshlrev_b32_e32 v50, 16, v50
	v_lshlrev_b64 v[170:171], 11, v[170:171]
	v_lshl_add_u64 v[170:171], s[6:7], 0, v[170:171]
	v_lshl_add_u64 v[170:171], v[170:171], 0, v[0:1]
	s_waitcnt vmcnt(0)
	v_fmac_f32_e32 v148, v184, v174
	v_mov_b32_e32 v174, v185
	v_fmac_f32_e32 v34, v184, v50
	v_mov_b32_e32 v50, v186
	s_nop 0
	v_lshlrev_b32_e32 v174, 16, v174
	v_mul_f32_e32 v148, v148, v174
	s_nop 0
	v_lshlrev_b32_e32 v50, 16, v50
	v_mul_f32_e32 v34, v34, v50
	v_bfe_u32 v50, v148, 16, 1
	v_add3_u32 v50, v148, v50, s79
	global_store_short_d16_hi v[170:171], v50, off offset:1024
	v_bfe_u32 v50, v34, 16, 1
	v_add3_u32 v34, v34, v50, s79
	global_store_short_d16_hi v[170:171], v34, off offset:1088
